# v48 + hand-written out-proj epilogue (x rows requested 4 steps ahead) + indexer K tiles via per-wave LDS-DMA ring two tiles ahead
# baseline (speedup 1.0000x reference)
.LBB0_404:
	s_lshl_b32 s12, s12, 10
	s_lshl_b32 s0, s13, 6
	s_add_i32 s1, s12, 0x400
	s_add_i32 s13, s0, 64
	s_min_u32 s1, s1, s13
	s_sub_i32 s1, s1, s12
	s_ashr_i32 s24, s1, 5
	s_cmp_lt_i32 s24, 1
	s_cbranch_scc1 .LBB0_407
	s_mul_i32 s13, s4, 0x3400000
	s_mul_hi_u32 s1, s4, 0x3400000
	s_add_u32 s14, s82, s13
	s_addc_u32 s15, s83, s1
	s_add_i32 s13, s0, s17
	v_or_b32_e32 v4, s13, v158
	v_mov_b64_e32 v[2:3], s[14:15]
	v_mad_u64_u32 v[4:5], s[0:1], v4, s18, v[2:3]
	s_or_b32 s25, s13, 2
	v_lshl_add_u64 v[4:5], v[4:5], 0, v[144:145]
	s_waitcnt vmcnt(30)
	v_or_b32_e32 v6, s25, v158
	v_lshl_add_u64 v[4:5], v[4:5], 0, v[148:149]
	v_mad_u64_u32 v[6:7], s[0:1], v6, s18, v[2:3]
	s_waitcnt vmcnt(22)
	v_lshl_add_u64 v[38:39], v[4:5], 0, s[6:7]
	v_add_co_u32_e32 v4, vcc, s19, v4
	v_lshl_add_u64 v[6:7], v[6:7], 0, v[144:145]
	s_nop 0
	v_addc_co_u32_e32 v5, vcc, 0, v5, vcc
	v_lshl_add_u64 v[6:7], v[6:7], 0, v[148:149]
	s_or_b32 s26, s13, 4
	global_load_dwordx4 v[66:69], v[38:39], off offset:64
	global_load_dwordx4 v[70:73], v[38:39], off offset:96
	v_lshl_add_u64 v[8:9], v[6:7], 0, s[6:7]
	global_load_dwordx4 v[74:77], v[4:5], off offset:2560
	global_load_dwordx4 v[78:81], v[8:9], off offset:32
	global_load_dwordx4 v[82:85], v[8:9], off offset:64
	global_load_dwordx4 v[86:89], v[8:9], off offset:96
	v_or_b32_e32 v4, s26, v158
	v_mad_u64_u32 v[4:5], s[0:1], v4, s18, v[2:3]
	v_add_co_u32_e32 v18, vcc, s19, v6
	v_lshl_add_u64 v[4:5], v[4:5], 0, v[144:145]
	s_nop 0
	v_addc_co_u32_e32 v19, vcc, 0, v7, vcc
	v_lshl_add_u64 v[4:5], v[4:5], 0, v[148:149]
	v_add_u32_e32 v6, s25, v142
	v_lshl_add_u64 v[20:21], v[4:5], 0, s[6:7]
	v_add_co_u32_e32 v4, vcc, s19, v4
	v_mad_i64_i32 v[22:23], s[0:1], v6, s18, v[2:3]
	v_add_u32_e32 v6, s13, v142
	v_addc_co_u32_e32 v5, vcc, 0, v5, vcc
	v_mad_i64_i32 v[10:11], s[0:1], v6, s18, v[2:3]
	v_add_co_u32_e32 v6, vcc, s20, v10
	s_or_b32 s25, s13, 6
	s_nop 0
	v_addc_co_u32_e32 v7, vcc, 0, v11, vcc
	v_or_b32_e32 v28, s25, v158
	v_add_co_u32_e32 v12, vcc, s20, v22
	v_mad_u64_u32 v[28:29], s[0:1], v28, s18, v[2:3]
	s_nop 0
	v_addc_co_u32_e32 v13, vcc, 0, v23, vcc
	v_lshl_add_u64 v[14:15], v[10:11], 0, s[10:11]
	v_lshl_add_u64 v[28:29], v[28:29], 0, v[144:145]
	global_load_dwordx4 v[6:9], v[6:7], off offset:640
	s_nop 0
	global_load_dwordx4 v[10:13], v[12:13], off offset:640
	s_nop 0
	global_load_dwordx4 v[14:17], v[14:15], off offset:16
	s_nop 0
	global_load_dwordx4 v[90:93], v[18:19], off offset:2560
	global_load_dwordx4 v[94:97], v[20:21], off offset:32
	global_load_dwordx4 v[98:101], v[20:21], off offset:64
	global_load_dwordx4 v[102:105], v[20:21], off offset:96
	v_add_u32_e32 v18, s26, v142
	v_lshl_add_u64 v[34:35], v[28:29], 0, v[148:149]
	v_add_u32_e32 v28, s25, v142
	v_mad_i64_i32 v[26:27], s[0:1], v18, s18, v[2:3]
	v_mad_i64_i32 v[2:3], s[0:1], v28, s18, v[2:3]
	v_add_co_u32_e32 v18, vcc, s20, v26
	v_add_co_u32_e64 v28, s[0:1], s20, v2
	s_nop 0
	v_addc_co_u32_e32 v19, vcc, 0, v27, vcc
	v_lshl_add_u64 v[22:23], v[22:23], 0, s[10:11]
	v_addc_co_u32_e64 v29, s[0:1], 0, v3, s[0:1]
	v_lshl_add_u64 v[30:31], v[26:27], 0, s[10:11]
	global_load_dwordx4 v[18:21], v[18:19], off offset:640
	s_nop 0
	global_load_dwordx4 v[22:25], v[22:23], off offset:16
	v_lshl_add_u64 v[36:37], v[34:35], 0, s[6:7]
	global_load_dwordx4 v[26:29], v[28:29], off offset:640
	s_nop 0
	global_load_dwordx4 v[30:33], v[30:31], off offset:16
	s_nop 0
	global_load_dwordx4 v[106:109], v[4:5], off offset:2560
	global_load_dwordx4 v[110:113], v[36:37], off offset:32
	global_load_dwordx4 v[114:117], v[36:37], off offset:64
	global_load_dwordx4 v[118:121], v[36:37], off offset:96
	v_or_b32_e32 v4, s12, v146
	v_mul_u32_u24_e32 v4, 0x1a00, v4
	v_mov_b32_e32 v5, v145
	v_add_co_u32_e32 v34, vcc, s19, v34
	v_lshl_add_u64 v[4:5], v[4:5], 1, s[14:15]
	s_nop 0
	v_addc_co_u32_e32 v35, vcc, 0, v35, vcc
	v_lshl_add_u64 v[4:5], v[4:5], 0, v[148:149]
	v_lshl_add_u64 v[2:3], v[2:3], 0, s[10:11]
	v_lshl_add_u64 v[152:153], v[4:5], 0, s[8:9]
	global_load_dwordx4 v[122:125], v[34:35], off offset:2560
	s_nop 0
	global_load_dwordx4 v[34:37], v[2:3], off offset:16
	global_load_dwordx4 v[126:129], v[38:39], off offset:32
	global_load_dwordx4 v[130:133], v[152:153], off offset:96
	global_load_dwordx4 v[134:137], v[152:153], off offset:64
	global_load_dwordx4 v[138:141], v[152:153], off offset:32
	v_add_co_u32_e32 v2, vcc, s20, v4
	s_lshl_b64 s[14:15], s[4:5], 12
	s_nop 0
	v_addc_co_u32_e32 v3, vcc, 0, v5, vcc
	global_load_dwordx4 v[2:5], v[2:3], off offset:512
	s_add_u32 s14, s13, s14
	s_addc_u32 s15, 0, s15
	v_lshl_add_u64 v[38:39], s[14:15], 0, v[142:143]
	v_lshlrev_b64 v[38:39], 14, v[38:39]
	s_mov_b32 s13, s5
	v_lshl_add_u64 v[38:39], s[84:85], 0, v[38:39]
	s_mov_b32 s0, 0
	v_lshl_add_u64 v[38:39], s[12:13], 2, v[38:39]
	v_mov_b32_e32 v151, v145
	v_lshl_add_u64 v[154:155], v[38:39], 0, v[150:151]
	s_mov_b32 s4, s0
	s_waitcnt vmcnt(20)
	v_lshlrev_b32_e32 v177, 16, v10
	s_waitcnt vmcnt(19)
	v_lshlrev_b32_e32 v168, 16, v14
	v_and_b32_e32 v169, 0xffff0000, v14
	v_lshlrev_b32_e32 v170, 16, v15
	v_lshlrev_b32_e32 v151, 16, v6
	v_and_b32_e32 v161, 0xffff0000, v6
	v_lshlrev_b32_e32 v162, 16, v7
	v_and_b32_e32 v163, 0xffff0000, v7
	v_lshlrev_b32_e32 v164, 16, v8
	v_and_b32_e32 v165, 0xffff0000, v8
	v_lshlrev_b32_e32 v166, 16, v9
	v_and_b32_e32 v167, 0xffff0000, v9
	v_and_b32_e32 v171, 0xffff0000, v15
	v_lshlrev_b32_e32 v172, 16, v16
	v_and_b32_e32 v173, 0xffff0000, v16
	v_lshlrev_b32_e32 v174, 16, v17
	v_and_b32_e32 v176, 0xffff0000, v17
	v_and_b32_e32 v178, 0xffff0000, v10
	v_lshlrev_b32_e32 v179, 16, v11
	v_and_b32_e32 v180, 0xffff0000, v11
	v_lshlrev_b32_e32 v181, 16, v12
	v_and_b32_e32 v182, 0xffff0000, v12
	v_lshlrev_b32_e32 v183, 16, v13
	v_and_b32_e32 v184, 0xffff0000, v13
	s_waitcnt vmcnt(13)
	v_lshlrev_b32_e32 v185, 16, v22
	v_and_b32_e32 v186, 0xffff0000, v22
	v_lshlrev_b32_e32 v187, 16, v23
	v_and_b32_e32 v188, 0xffff0000, v23
	v_lshlrev_b32_e32 v189, 16, v24
	v_and_b32_e32 v190, 0xffff0000, v24
	v_lshlrev_b32_e32 v191, 16, v25
	v_and_b32_e32 v192, 0xffff0000, v25
	v_lshlrev_b32_e32 v193, 16, v18
	v_and_b32_e32 v194, 0xffff0000, v18
	v_lshlrev_b32_e32 v195, 16, v19
	v_and_b32_e32 v196, 0xffff0000, v19
	v_lshlrev_b32_e32 v197, 16, v20
	v_and_b32_e32 v198, 0xffff0000, v20
	v_lshlrev_b32_e32 v199, 16, v21
	v_and_b32_e32 v200, 0xffff0000, v21
	s_waitcnt vmcnt(11)
	v_lshlrev_b32_e32 v201, 16, v30
	v_and_b32_e32 v202, 0xffff0000, v30
	v_lshlrev_b32_e32 v203, 16, v31
	v_and_b32_e32 v204, 0xffff0000, v31
	v_lshlrev_b32_e32 v205, 16, v32
	v_and_b32_e32 v206, 0xffff0000, v32
	v_lshlrev_b32_e32 v207, 16, v33
	v_and_b32_e32 v208, 0xffff0000, v33
	v_lshlrev_b32_e32 v209, 16, v26
	v_and_b32_e32 v210, 0xffff0000, v26
	v_lshlrev_b32_e32 v211, 16, v27
	v_and_b32_e32 v212, 0xffff0000, v27
	v_lshlrev_b32_e32 v213, 16, v28
	v_and_b32_e32 v214, 0xffff0000, v28
	v_lshlrev_b32_e32 v215, 16, v29
	v_and_b32_e32 v216, 0xffff0000, v29
	s_waitcnt vmcnt(5)
	v_lshlrev_b32_e32 v217, 16, v34
	v_and_b32_e32 v218, 0xffff0000, v34
	v_lshlrev_b32_e32 v219, 16, v35
	v_and_b32_e32 v220, 0xffff0000, v35
	v_lshlrev_b32_e32 v221, 16, v36
	v_and_b32_e32 v222, 0xffff0000, v36
	v_lshlrev_b32_e32 v223, 16, v37
	v_and_b32_e32 v224, 0xffff0000, v37
	v_mbcnt_lo_u32_b32 v243, -1, 0
	v_mbcnt_hi_u32_b32 v243, -1, v243
	v_lshrrev_b32_e32 v246, 3, v243
	v_and_b32_e32 v247, 31, v243
	v_sub_u32_e32 v247, v246, v247
	v_mul_i32_i24_e32 v244, 0x3400, v247
	v_lshrrev_b32_e32 v246, 1, v246
	v_and_b32_e32 v247, 7, v243
	v_xor_b32_e32 v246, v246, v247
	v_lshrrev_b32_e32 v247, 5, v243
	v_sub_u32_e32 v246, v246, v247
	v_lshl_add_u32 v244, v246, 4, v244
	v_ashrrev_i32_e32 v245, 31, v244
	s_mul_i32 s27, s76, 0x3000
	v_and_b32_e32 v246, 31, v243
	v_lshlrev_b32_e32 v225, 7, v246
	v_bfe_u32 v247, v246, 2, 2
	v_lshl_add_u32 v225, v247, 5, v225
	v_bfe_u32 v247, v246, 1, 1
	v_lshrrev_b32_e32 v246, 5, v243
	v_xor_b32_e32 v246, v246, v247
	v_lshl_add_u32 v225, v246, 4, v225
	v_add_u32_e32 v225, s27, v225
	s_mov_b32 s28, 0x1a000
	s_mov_b32 s29, 0
	s_add_i32 s31, s24, -1
	s_min_i32 s30, s31, 1
	v_mad_u64_u32 v[246:247], s[32:33], s30, v159, v[152:153]
	s_add_u32 m0, s27, 0x1000
	v_lshl_add_u64 v[246:247], v[246:247], 0, v[244:245]
	global_load_lds_dwordx4 v[246:247], off
	s_add_u32 m0, m0, 0x400
	v_lshl_add_u64 v[246:247], v[246:247], 0, s[28:29]
	v_xor_b32_e32 v246, 64, v246
	global_load_lds_dwordx4 v[246:247], off
	s_add_u32 m0, m0, 0x400
	v_lshl_add_u64 v[246:247], v[246:247], 0, s[28:29]
	v_xor_b32_e32 v246, 64, v246
	global_load_lds_dwordx4 v[246:247], off
	s_add_u32 m0, m0, 0x400
	v_lshl_add_u64 v[246:247], v[246:247], 0, s[28:29]
	v_xor_b32_e32 v246, 64, v246
	global_load_lds_dwordx4 v[246:247], off
	s_mov_b32 s34, 0x1000
	s_waitcnt vmcnt(0)
.LBB0_406:
	s_waitcnt lgkmcnt(3)
	v_mfma_f32_32x32x16_bf16 v[50:65], v[74:77], v[2:5], 0
	s_add_i32 s1, s0, 1
	s_mov_b32 s35, s34
	s_add_u32 s34, s34, 0x1000
	s_cmp_eq_u32 s34, 0x3000
	s_cselect_b32 s34, 0, s34
	s_add_i32 s30, s1, 1
	s_add_i32 s31, s24, -1
	s_min_i32 s30, s30, s31
	v_mad_u64_u32 v[246:247], s[32:33], s30, v159, v[152:153]
	v_add_u32_e32 v243, s35, v225
	s_mov_b32 s0, s1
	v_mfma_f32_32x32x16_bf16 v[34:49], v[90:93], v[2:5], 0
	v_mfma_f32_32x32x16_bf16 v[18:33], v[106:109], v[2:5], 0
	v_mfma_f32_32x32x16_bf16 v[2:17], v[122:125], v[2:5], 0
	s_waitcnt lgkmcnt(2)
	v_mfma_f32_32x32x16_bf16 v[50:65], v[126:129], v[138:141], v[50:65]
	v_mfma_f32_32x32x16_bf16 v[34:49], v[78:81], v[138:141], v[34:49]
	v_mfma_f32_32x32x16_bf16 v[18:33], v[94:97], v[138:141], v[18:33]
	v_mfma_f32_32x32x16_bf16 v[2:17], v[110:113], v[138:141], v[2:17]
	s_add_u32 m0, s27, s34
	v_lshl_add_u64 v[246:247], v[246:247], 0, v[244:245]
	global_load_lds_dwordx4 v[246:247], off
	s_add_u32 m0, m0, 0x400
	v_lshl_add_u64 v[246:247], v[246:247], 0, s[28:29]
	v_xor_b32_e32 v246, 64, v246
	global_load_lds_dwordx4 v[246:247], off
	s_add_u32 m0, m0, 0x400
	v_lshl_add_u64 v[246:247], v[246:247], 0, s[28:29]
	v_xor_b32_e32 v246, 64, v246
	global_load_lds_dwordx4 v[246:247], off
	s_add_u32 m0, m0, 0x400
	v_lshl_add_u64 v[246:247], v[246:247], 0, s[28:29]
	v_xor_b32_e32 v246, 64, v246
	global_load_lds_dwordx4 v[246:247], off
	s_waitcnt lgkmcnt(0)
	v_mfma_f32_32x32x16_bf16 v[50:65], v[66:69], v[134:137], v[50:65]
	v_mfma_f32_32x32x16_bf16 v[34:49], v[82:85], v[134:137], v[34:49]
	v_mfma_f32_32x32x16_bf16 v[18:33], v[98:101], v[134:137], v[18:33]
	v_mfma_f32_32x32x16_bf16 v[2:17], v[114:117], v[134:137], v[2:17]
	v_lshl_add_u64 v[134:135], s[4:5], 2, v[154:155]
	v_add_co_u32_e32 v136, vcc, s21, v134
	s_add_i32 s4, s4, 32
	s_nop 0
	v_addc_co_u32_e32 v137, vcc, 0, v135, vcc
	v_add_co_u32_e32 v238, vcc, s22, v134
	v_mfma_f32_32x32x16_bf16 v[50:65], v[70:73], v[130:133], v[50:65]
	s_nop 0
	v_addc_co_u32_e32 v239, vcc, 0, v135, vcc
	v_add_co_u32_e32 v240, vcc, 0x18000, v134
	s_cmp_lg_u32 s24, s1
	s_nop 0
	v_addc_co_u32_e32 v241, vcc, 0, v135, vcc
	v_mfma_f32_32x32x16_bf16 v[34:49], v[86:89], v[130:133], v[34:49]
	s_nop 4
	v_med3_f32 v50, v50, 0, v160
	v_med3_f32 v51, v51, 0, v160
	v_fma_f32 v50, v151, v50, 0
	v_med3_f32 v52, v52, 0, v160
	v_fmac_f32_e32 v50, v161, v51
	v_med3_f32 v53, v53, 0, v160
	v_fmac_f32_e32 v50, v162, v52
	v_mfma_f32_32x32x16_bf16 v[18:33], v[102:105], v[130:133], v[18:33]
	v_med3_f32 v34, v34, 0, v160
	v_med3_f32 v35, v35, 0, v160
	v_fma_f32 v34, v177, v34, 0
	v_med3_f32 v36, v36, 0, v160
	v_fmac_f32_e32 v34, v178, v35
	v_med3_f32 v37, v37, 0, v160
	v_fmac_f32_e32 v34, v179, v36
	v_mfma_f32_32x32x16_bf16 v[2:17], v[118:121], v[130:133], v[2:17]
	s_nop 3
	v_med3_f32 v18, v18, 0, v160
	v_med3_f32 v19, v19, 0, v160
	v_fma_f32 v18, v193, v18, 0
	v_med3_f32 v20, v20, 0, v160
	v_fmac_f32_e32 v18, v194, v19
	v_med3_f32 v21, v21, 0, v160
	v_fmac_f32_e32 v18, v195, v20
	s_nop 0
	v_med3_f32 v2, v2, 0, v160
	v_med3_f32 v3, v3, 0, v160
	v_fma_f32 v2, v209, v2, 0
	v_med3_f32 v4, v4, 0, v160
	v_fmac_f32_e32 v2, v210, v3
	v_med3_f32 v5, v5, 0, v160
	v_fmac_f32_e32 v2, v211, v4
	v_med3_f32 v54, v54, 0, v160
	v_med3_f32 v38, v38, 0, v160
	v_med3_f32 v22, v22, 0, v160
	v_med3_f32 v6, v6, 0, v160
	v_fmac_f32_e32 v50, v163, v53
	v_fmac_f32_e32 v34, v180, v37
	v_fmac_f32_e32 v18, v196, v21
	v_fmac_f32_e32 v2, v212, v5
	v_med3_f32 v55, v55, 0, v160
	v_med3_f32 v39, v39, 0, v160
	v_med3_f32 v23, v23, 0, v160
	v_med3_f32 v7, v7, 0, v160
	v_fmac_f32_e32 v50, v164, v54
	v_fmac_f32_e32 v34, v181, v38
	v_fmac_f32_e32 v18, v197, v22
	v_fmac_f32_e32 v2, v213, v6
	v_med3_f32 v56, v56, 0, v160
	v_med3_f32 v40, v40, 0, v160
	v_med3_f32 v24, v24, 0, v160
	v_med3_f32 v8, v8, 0, v160
	v_fmac_f32_e32 v50, v165, v55
	v_fmac_f32_e32 v34, v182, v39
	v_fmac_f32_e32 v18, v198, v23
	v_fmac_f32_e32 v2, v214, v7
	v_med3_f32 v57, v57, 0, v160
	v_med3_f32 v41, v41, 0, v160
	v_med3_f32 v25, v25, 0, v160
	v_med3_f32 v9, v9, 0, v160
	v_fmac_f32_e32 v50, v166, v56
	v_fmac_f32_e32 v34, v183, v40
	v_fmac_f32_e32 v18, v199, v24
	v_fmac_f32_e32 v2, v215, v8
	v_med3_f32 v58, v58, 0, v160
	v_med3_f32 v42, v42, 0, v160
	v_med3_f32 v26, v26, 0, v160
	v_med3_f32 v10, v10, 0, v160
	v_fmac_f32_e32 v50, v167, v57
	v_fmac_f32_e32 v34, v184, v41
	v_fmac_f32_e32 v18, v200, v25
	v_fmac_f32_e32 v2, v216, v9
	v_med3_f32 v59, v59, 0, v160
	v_med3_f32 v43, v43, 0, v160
	v_med3_f32 v27, v27, 0, v160
	v_med3_f32 v11, v11, 0, v160
	v_fmac_f32_e32 v50, v168, v58
	v_fmac_f32_e32 v34, v185, v42
	v_fmac_f32_e32 v18, v201, v26
	v_fmac_f32_e32 v2, v217, v10
	v_med3_f32 v60, v60, 0, v160
	v_med3_f32 v44, v44, 0, v160
	v_med3_f32 v28, v28, 0, v160
	v_med3_f32 v12, v12, 0, v160
	v_fmac_f32_e32 v50, v169, v59
	v_fmac_f32_e32 v34, v186, v43
	v_fmac_f32_e32 v18, v202, v27
	v_fmac_f32_e32 v2, v218, v11
	v_med3_f32 v61, v61, 0, v160
	v_med3_f32 v45, v45, 0, v160
	v_med3_f32 v29, v29, 0, v160
	v_med3_f32 v13, v13, 0, v160
	v_fmac_f32_e32 v50, v170, v60
	v_fmac_f32_e32 v34, v187, v44
	v_fmac_f32_e32 v18, v203, v28
	v_fmac_f32_e32 v2, v219, v12
	v_med3_f32 v62, v62, 0, v160
	v_med3_f32 v46, v46, 0, v160
	v_med3_f32 v30, v30, 0, v160
	v_med3_f32 v14, v14, 0, v160
	v_fmac_f32_e32 v50, v171, v61
	v_fmac_f32_e32 v34, v188, v45
	v_fmac_f32_e32 v18, v204, v29
	v_fmac_f32_e32 v2, v220, v13
	v_med3_f32 v63, v63, 0, v160
	v_med3_f32 v47, v47, 0, v160
	v_med3_f32 v31, v31, 0, v160
	v_med3_f32 v15, v15, 0, v160
	v_fmac_f32_e32 v50, v172, v62
	v_fmac_f32_e32 v34, v189, v46
	v_fmac_f32_e32 v18, v205, v30
	v_fmac_f32_e32 v2, v221, v14
	v_med3_f32 v64, v64, 0, v160
	v_med3_f32 v48, v48, 0, v160
	v_med3_f32 v32, v32, 0, v160
	v_med3_f32 v16, v16, 0, v160
	v_fmac_f32_e32 v50, v173, v63
	v_fmac_f32_e32 v34, v190, v47
	v_fmac_f32_e32 v18, v206, v31
	v_fmac_f32_e32 v2, v222, v15
	v_med3_f32 v65, v65, 0, v160
	v_med3_f32 v49, v49, 0, v160
	v_med3_f32 v33, v33, 0, v160
	v_med3_f32 v17, v17, 0, v160
	v_fmac_f32_e32 v50, v174, v64
	v_fmac_f32_e32 v34, v191, v48
	v_fmac_f32_e32 v18, v207, v32
	v_fmac_f32_e32 v2, v223, v16
	v_fmac_f32_e32 v50, v176, v65
	v_fmac_f32_e32 v34, v192, v49
	v_fmac_f32_e32 v18, v208, v33
	v_fmac_f32_e32 v2, v224, v17
	v_mul_f32_e32 v3, 0x3d000000, v50
	v_mul_f32_e32 v4, 0x3d000000, v34
	v_mul_f32_e32 v5, 0x3d000000, v18
	v_mul_f32_e32 v2, 0x3d000000, v2
	global_store_dword v[134:135], v3, off
	global_store_dword v[136:137], v4, off
	global_store_dword v[238:239], v5, off
	global_store_dword v[240:241], v2, off
	s_waitcnt vmcnt(12)
	ds_read_b128 v[2:5], v243
	v_xor_b32_e32 v246, 32, v243
	ds_read_b128 v[138:141], v246
	v_xor_b32_e32 v247, 64, v243
	ds_read_b128 v[134:137], v247
	v_xor_b32_e32 v246, 0x60, v243
	ds_read_b128 v[130:133], v246
	s_cbranch_scc1 .LBB0_406
.LBB0_407:
	s_waitcnt vmcnt(0) lgkmcnt(0)
	s_barrier
	s_and_saveexec_b64 s[0:1], s[2:3]
	s_cbranch_execz .LBB0_393
	s_mov_b64 s[14:15], exec
	v_mbcnt_lo_u32_b32 v2, s14, 0
	v_mbcnt_hi_u32_b32 v2, s15, v2
	v_cmp_eq_u32_e32 vcc, 0, v2
	s_and_saveexec_b64 s[12:13], vcc
	s_cbranch_execz .LBB0_392
	s_bcnt1_i32_b64 s4, s[14:15]
	v_mov_b32_e32 v3, s4
	global_atomic_add v3, v145, v3, s[54:55] offset:256 sc0
	s_branch .LBB0_392

.LBB0_1235:
	s_ashr_i32 s19, s26, 31
	s_lshr_b32 s19, s19, 28
	s_add_i32 s19, s26, s19
	s_ashr_i32 s19, s19, 4
	s_mul_hi_i32 s21, s19, 0x18000
	s_mul_i32 s19, s19, 0x18000
	s_add_u32 s19, s78, s19
	v_lshl_or_b32 v146, s56, 8, v157
	s_addc_u32 s21, s79, s21
	s_add_u32 s30, s19, 0x8000
	v_ashrrev_i32_e32 v147, 31, v146
	v_lshl_add_u32 v154, s26, 8, v1
	s_addc_u32 s31, s21, 0
	v_lshlrev_b64 v[150:151], 2, v[146:147]
	v_ashrrev_i32_e32 v155, 31, v154
	v_lshl_add_u64 v[152:153], s[30:31], 0, v[150:151]
	v_lshl_add_u64 v[148:149], v[154:155], 2, s[72:73]
	v_lshl_add_u64 v[150:151], s[6:7], 0, v[150:151]
	v_readlane_b32 s80, v242, 11
	v_readlane_b32 s81, v242, 12
	s_mov_b32 s36, 0x40000
	s_mov_b32 s37, 0
	s_mov_b32 s38, 0x140000
	s_mov_b32 s39, 0
	s_mov_b32 s58, 0x20000
	s_mov_b32 s59, 0
	s_mov_b32 s60, 0xa0000
	s_mov_b32 s61, 0
	v_lshlrev_b64 v[162:163], 12, v[154:155]
	v_lshl_add_u64 v[162:163], v[162:163], 0, v[146:147]
	global_load_dword v168, v[148:149], off
	global_load_dword v169, v[148:149], off offset:64
	global_load_dword v170, v[148:149], off offset:128
	global_load_dword v171, v[148:149], off offset:192
	global_load_dword v172, v[148:149], off offset:512
	global_load_dword v173, v[148:149], off offset:576
	global_load_dword v174, v[148:149], off offset:640
	global_load_dword v161, v[148:149], off offset:704
	global_load_dwordx4 v[176:179], v[152:153], off
	global_load_dwordx4 v[180:183], v[152:153], off offset:16
	global_load_dwordx4 v[184:187], v[152:153], off offset:512
	global_load_dwordx4 v[188:191], v[152:153], off offset:528
	global_load_dwordx4 v[192:195], v[150:151], off
	global_load_dwordx4 v[196:199], v[150:151], off offset:16
	global_load_dwordx4 v[200:203], v[150:151], off offset:512
	global_load_dwordx4 v[204:207], v[150:151], off offset:528
	v_lshl_add_u64 v[164:165], v[162:163], 2, s[80:81]
	v_lshl_add_u64 v[166:167], v[162:163], 1, s[28:29]
	global_load_dwordx4 v[208:211], v[164:165], off
	global_load_dwordx4 v[212:215], v[164:165], off offset:16
	global_load_dwordx4 v[216:219], v[164:165], off offset:512
	global_load_dwordx4 v[220:223], v[164:165], off offset:528
	v_lshl_add_u64 v[164:165], v[164:165], 0, s[36:37]
	global_load_dwordx4 v[224:227], v[164:165], off
	global_load_dwordx4 v[228:231], v[164:165], off offset:16
	global_load_dwordx4 v[232:235], v[164:165], off offset:512
	global_load_dwordx4 v[236:239], v[164:165], off offset:528
	v_cvt_f32_i32_e32 v126, v126
	v_cvt_f32_i32_e32 v127, v127
	v_cvt_f32_i32_e32 v128, v128
	v_cvt_f32_i32_e32 v129, v129
	v_cvt_f32_i32_e32 v122, v122
	v_cvt_f32_i32_e32 v123, v123
	v_cvt_f32_i32_e32 v124, v124
	v_cvt_f32_i32_e32 v125, v125
	v_mov_b32_e32 v240, v168
	s_waitcnt vmcnt(6)
	v_pk_mul_f32 v[176:177], v[176:177], v[192:193]
	v_pk_mul_f32 v[178:179], v[178:179], v[194:195]
	v_pk_mul_f32 v[180:181], v[180:181], v[196:197]
	v_pk_mul_f32 v[182:183], v[182:183], v[198:199]
	v_pk_mul_f32 v[184:185], v[184:185], v[200:201]
	v_pk_mul_f32 v[186:187], v[186:187], v[202:203]
	v_pk_mul_f32 v[188:189], v[188:189], v[204:205]
	v_pk_mul_f32 v[190:191], v[190:191], v[206:207]
	v_mov_b32_e32 v240, v168
	v_pk_mul_f32 v[126:127], v[240:241], v[126:127] op_sel_hi:[0,1]
	v_pk_mul_f32 v[128:129], v[240:241], v[128:129] op_sel_hi:[0,1]
	v_pk_mul_f32 v[122:123], v[240:241], v[122:123] op_sel_hi:[0,1]
	v_pk_mul_f32 v[124:125], v[240:241], v[124:125] op_sel_hi:[0,1]
	v_pk_fma_f32 v[126:127], v[176:177], v[126:127], v[208:209]
	v_pk_fma_f32 v[128:129], v[178:179], v[128:129], v[210:211]
	v_pk_fma_f32 v[122:123], v[180:181], v[122:123], v[212:213]
	v_pk_fma_f32 v[124:125], v[182:183], v[124:125], v[214:215]
	v_cvt_pk_bf16_f32 v150, v126, v127
	v_cvt_pk_bf16_f32 v151, v128, v129
	v_cvt_pk_bf16_f32 v152, v122, v123
	v_cvt_pk_bf16_f32 v153, v124, v125
	global_store_dwordx4 v[166:167], v[150:153], off
	v_lshl_add_u64 v[164:165], v[164:165], 0, s[36:37]
	global_load_dwordx4 v[126:129], v[164:165], off
	global_load_dwordx4 v[122:125], v[164:165], off offset:16
	v_cvt_f32_i32_e32 v118, v118
	v_cvt_f32_i32_e32 v119, v119
	v_cvt_f32_i32_e32 v120, v120
	v_cvt_f32_i32_e32 v121, v121
	v_cvt_f32_i32_e32 v114, v114
	v_cvt_f32_i32_e32 v115, v115
	v_cvt_f32_i32_e32 v116, v116
	v_cvt_f32_i32_e32 v117, v117
	s_waitcnt vmcnt(7)
	v_pk_mul_f32 v[118:119], v[240:241], v[118:119] op_sel_hi:[0,1]
	v_pk_mul_f32 v[120:121], v[240:241], v[120:121] op_sel_hi:[0,1]
	v_pk_mul_f32 v[114:115], v[240:241], v[114:115] op_sel_hi:[0,1]
	v_pk_mul_f32 v[116:117], v[240:241], v[116:117] op_sel_hi:[0,1]
	v_pk_fma_f32 v[118:119], v[184:185], v[118:119], v[216:217]
	v_pk_fma_f32 v[120:121], v[186:187], v[120:121], v[218:219]
	v_pk_fma_f32 v[114:115], v[188:189], v[114:115], v[220:221]
	v_pk_fma_f32 v[116:117], v[190:191], v[116:117], v[222:223]
	v_cvt_pk_bf16_f32 v244, v118, v119
	v_cvt_pk_bf16_f32 v245, v120, v121
	v_cvt_pk_bf16_f32 v246, v114, v115
	v_cvt_pk_bf16_f32 v247, v116, v117
	global_store_dwordx4 v[166:167], v[244:247], off offset:256
	global_load_dwordx4 v[118:121], v[164:165], off offset:512
	global_load_dwordx4 v[114:117], v[164:165], off offset:528
	v_cvt_f32_i32_e32 v110, v110
	v_cvt_f32_i32_e32 v111, v111
	v_cvt_f32_i32_e32 v112, v112
	v_cvt_f32_i32_e32 v113, v113
	v_cvt_f32_i32_e32 v106, v106
	v_cvt_f32_i32_e32 v107, v107
	v_cvt_f32_i32_e32 v108, v108
	v_cvt_f32_i32_e32 v109, v109
	v_mov_b32_e32 v240, v169
	s_waitcnt vmcnt(8)
	v_pk_mul_f32 v[110:111], v[240:241], v[110:111] op_sel_hi:[0,1]
	v_pk_mul_f32 v[112:113], v[240:241], v[112:113] op_sel_hi:[0,1]
	v_pk_mul_f32 v[106:107], v[240:241], v[106:107] op_sel_hi:[0,1]
	v_pk_mul_f32 v[108:109], v[240:241], v[108:109] op_sel_hi:[0,1]
	v_pk_fma_f32 v[110:111], v[176:177], v[110:111], v[224:225]
	v_pk_fma_f32 v[112:113], v[178:179], v[112:113], v[226:227]
	v_pk_fma_f32 v[106:107], v[180:181], v[106:107], v[228:229]
	v_pk_fma_f32 v[108:109], v[182:183], v[108:109], v[230:231]
	v_cvt_pk_bf16_f32 v150, v110, v111
	v_cvt_pk_bf16_f32 v151, v112, v113
	v_cvt_pk_bf16_f32 v152, v106, v107
	v_cvt_pk_bf16_f32 v153, v108, v109
	v_lshl_add_u64 v[166:167], v[166:167], 0, s[58:59]
	global_store_dwordx4 v[166:167], v[150:153], off
	v_lshl_add_u64 v[164:165], v[164:165], 0, s[36:37]
	global_load_dwordx4 v[110:113], v[164:165], off
	global_load_dwordx4 v[106:109], v[164:165], off offset:16
	v_cvt_f32_i32_e32 v102, v102
	v_cvt_f32_i32_e32 v103, v103
	v_cvt_f32_i32_e32 v104, v104
	v_cvt_f32_i32_e32 v105, v105
	v_cvt_f32_i32_e32 v98, v98
	v_cvt_f32_i32_e32 v99, v99
	v_cvt_f32_i32_e32 v100, v100
	v_cvt_f32_i32_e32 v101, v101
	s_waitcnt vmcnt(9)
	v_pk_mul_f32 v[102:103], v[240:241], v[102:103] op_sel_hi:[0,1]
	v_pk_mul_f32 v[104:105], v[240:241], v[104:105] op_sel_hi:[0,1]
	v_pk_mul_f32 v[98:99], v[240:241], v[98:99] op_sel_hi:[0,1]
	v_pk_mul_f32 v[100:101], v[240:241], v[100:101] op_sel_hi:[0,1]
	v_pk_fma_f32 v[102:103], v[184:185], v[102:103], v[232:233]
	v_pk_fma_f32 v[104:105], v[186:187], v[104:105], v[234:235]
	v_pk_fma_f32 v[98:99], v[188:189], v[98:99], v[236:237]
	v_pk_fma_f32 v[100:101], v[190:191], v[100:101], v[238:239]
	v_cvt_pk_bf16_f32 v244, v102, v103
	v_cvt_pk_bf16_f32 v245, v104, v105
	v_cvt_pk_bf16_f32 v246, v98, v99
	v_cvt_pk_bf16_f32 v247, v100, v101
	global_store_dwordx4 v[166:167], v[244:247], off offset:256
	global_load_dwordx4 v[102:105], v[164:165], off offset:512
	global_load_dwordx4 v[98:101], v[164:165], off offset:528
	v_cvt_f32_i32_e32 v94, v94
	v_cvt_f32_i32_e32 v95, v95
	v_cvt_f32_i32_e32 v96, v96
	v_cvt_f32_i32_e32 v97, v97
	v_cvt_f32_i32_e32 v90, v90
	v_cvt_f32_i32_e32 v91, v91
	v_cvt_f32_i32_e32 v92, v92
	v_cvt_f32_i32_e32 v93, v93
	v_mov_b32_e32 v240, v170
	s_waitcnt vmcnt(9)
	v_pk_mul_f32 v[94:95], v[240:241], v[94:95] op_sel_hi:[0,1]
	v_pk_mul_f32 v[96:97], v[240:241], v[96:97] op_sel_hi:[0,1]
	v_pk_mul_f32 v[90:91], v[240:241], v[90:91] op_sel_hi:[0,1]
	v_pk_mul_f32 v[92:93], v[240:241], v[92:93] op_sel_hi:[0,1]
	v_pk_fma_f32 v[94:95], v[176:177], v[94:95], v[126:127]
	v_pk_fma_f32 v[96:97], v[178:179], v[96:97], v[128:129]
	v_pk_fma_f32 v[90:91], v[180:181], v[90:91], v[122:123]
	v_pk_fma_f32 v[92:93], v[182:183], v[92:93], v[124:125]
	v_cvt_pk_bf16_f32 v150, v94, v95
	v_cvt_pk_bf16_f32 v151, v96, v97
	v_cvt_pk_bf16_f32 v152, v90, v91
	v_cvt_pk_bf16_f32 v153, v92, v93
	v_lshl_add_u64 v[166:167], v[166:167], 0, s[58:59]
	global_store_dwordx4 v[166:167], v[150:153], off
	v_lshl_add_u64 v[164:165], v[164:165], 0, s[38:39]
	global_load_dwordx4 v[94:97], v[164:165], off
	global_load_dwordx4 v[90:93], v[164:165], off offset:16
	v_cvt_f32_i32_e32 v86, v86
	v_cvt_f32_i32_e32 v87, v87
	v_cvt_f32_i32_e32 v88, v88
	v_cvt_f32_i32_e32 v89, v89
	v_cvt_f32_i32_e32 v82, v82
	v_cvt_f32_i32_e32 v83, v83
	v_cvt_f32_i32_e32 v84, v84
	v_cvt_f32_i32_e32 v85, v85
	s_waitcnt vmcnt(9)
	v_pk_mul_f32 v[86:87], v[240:241], v[86:87] op_sel_hi:[0,1]
	v_pk_mul_f32 v[88:89], v[240:241], v[88:89] op_sel_hi:[0,1]
	v_pk_mul_f32 v[82:83], v[240:241], v[82:83] op_sel_hi:[0,1]
	v_pk_mul_f32 v[84:85], v[240:241], v[84:85] op_sel_hi:[0,1]
	v_pk_fma_f32 v[86:87], v[184:185], v[86:87], v[118:119]
	v_pk_fma_f32 v[88:89], v[186:187], v[88:89], v[120:121]
	v_pk_fma_f32 v[82:83], v[188:189], v[82:83], v[114:115]
	v_pk_fma_f32 v[84:85], v[190:191], v[84:85], v[116:117]
	v_cvt_pk_bf16_f32 v244, v86, v87
	v_cvt_pk_bf16_f32 v245, v88, v89
	v_cvt_pk_bf16_f32 v246, v82, v83
	v_cvt_pk_bf16_f32 v247, v84, v85
	global_store_dwordx4 v[166:167], v[244:247], off offset:256
	global_load_dwordx4 v[86:89], v[164:165], off offset:512
	global_load_dwordx4 v[82:85], v[164:165], off offset:528
	v_cvt_f32_i32_e32 v78, v78
	v_cvt_f32_i32_e32 v79, v79
	v_cvt_f32_i32_e32 v80, v80
	v_cvt_f32_i32_e32 v81, v81
	v_cvt_f32_i32_e32 v74, v74
	v_cvt_f32_i32_e32 v75, v75
	v_cvt_f32_i32_e32 v76, v76
	v_cvt_f32_i32_e32 v77, v77
	v_mov_b32_e32 v240, v171
	s_waitcnt vmcnt(9)
	v_pk_mul_f32 v[78:79], v[240:241], v[78:79] op_sel_hi:[0,1]
	v_pk_mul_f32 v[80:81], v[240:241], v[80:81] op_sel_hi:[0,1]
	v_pk_mul_f32 v[74:75], v[240:241], v[74:75] op_sel_hi:[0,1]
	v_pk_mul_f32 v[76:77], v[240:241], v[76:77] op_sel_hi:[0,1]
	v_pk_fma_f32 v[78:79], v[176:177], v[78:79], v[110:111]
	v_pk_fma_f32 v[80:81], v[178:179], v[80:81], v[112:113]
	v_pk_fma_f32 v[74:75], v[180:181], v[74:75], v[106:107]
	v_pk_fma_f32 v[76:77], v[182:183], v[76:77], v[108:109]
	v_cvt_pk_bf16_f32 v150, v78, v79
	v_cvt_pk_bf16_f32 v151, v80, v81
	v_cvt_pk_bf16_f32 v152, v74, v75
	v_cvt_pk_bf16_f32 v153, v76, v77
	v_lshl_add_u64 v[166:167], v[166:167], 0, s[58:59]
	global_store_dwordx4 v[166:167], v[150:153], off
	v_lshl_add_u64 v[164:165], v[164:165], 0, s[36:37]
	global_load_dwordx4 v[78:81], v[164:165], off
	global_load_dwordx4 v[74:77], v[164:165], off offset:16
	v_cvt_f32_i32_e32 v70, v70
	v_cvt_f32_i32_e32 v71, v71
	v_cvt_f32_i32_e32 v72, v72
	v_cvt_f32_i32_e32 v73, v73
	v_cvt_f32_i32_e32 v66, v66
	v_cvt_f32_i32_e32 v67, v67
	v_cvt_f32_i32_e32 v68, v68
	v_cvt_f32_i32_e32 v69, v69
	s_waitcnt vmcnt(9)
	v_pk_mul_f32 v[70:71], v[240:241], v[70:71] op_sel_hi:[0,1]
	v_pk_mul_f32 v[72:73], v[240:241], v[72:73] op_sel_hi:[0,1]
	v_pk_mul_f32 v[66:67], v[240:241], v[66:67] op_sel_hi:[0,1]
	v_pk_mul_f32 v[68:69], v[240:241], v[68:69] op_sel_hi:[0,1]
	v_pk_fma_f32 v[70:71], v[184:185], v[70:71], v[102:103]
	v_pk_fma_f32 v[72:73], v[186:187], v[72:73], v[104:105]
	v_pk_fma_f32 v[66:67], v[188:189], v[66:67], v[98:99]
	v_pk_fma_f32 v[68:69], v[190:191], v[68:69], v[100:101]
	v_cvt_pk_bf16_f32 v244, v70, v71
	v_cvt_pk_bf16_f32 v245, v72, v73
	v_cvt_pk_bf16_f32 v246, v66, v67
	v_cvt_pk_bf16_f32 v247, v68, v69
	global_store_dwordx4 v[166:167], v[244:247], off offset:256
	global_load_dwordx4 v[70:73], v[164:165], off offset:512
	global_load_dwordx4 v[66:69], v[164:165], off offset:528
	v_cvt_f32_i32_e32 v62, v62
	v_cvt_f32_i32_e32 v63, v63
	v_cvt_f32_i32_e32 v64, v64
	v_cvt_f32_i32_e32 v65, v65
	v_cvt_f32_i32_e32 v58, v58
	v_cvt_f32_i32_e32 v59, v59
	v_cvt_f32_i32_e32 v60, v60
	v_cvt_f32_i32_e32 v61, v61
	v_mov_b32_e32 v240, v172
	s_waitcnt vmcnt(9)
	v_pk_mul_f32 v[62:63], v[240:241], v[62:63] op_sel_hi:[0,1]
	v_pk_mul_f32 v[64:65], v[240:241], v[64:65] op_sel_hi:[0,1]
	v_pk_mul_f32 v[58:59], v[240:241], v[58:59] op_sel_hi:[0,1]
	v_pk_mul_f32 v[60:61], v[240:241], v[60:61] op_sel_hi:[0,1]
	v_pk_fma_f32 v[62:63], v[176:177], v[62:63], v[94:95]
	v_pk_fma_f32 v[64:65], v[178:179], v[64:65], v[96:97]
	v_pk_fma_f32 v[58:59], v[180:181], v[58:59], v[90:91]
	v_pk_fma_f32 v[60:61], v[182:183], v[60:61], v[92:93]
	v_cvt_pk_bf16_f32 v150, v62, v63
	v_cvt_pk_bf16_f32 v151, v64, v65
	v_cvt_pk_bf16_f32 v152, v58, v59
	v_cvt_pk_bf16_f32 v153, v60, v61
	v_lshl_add_u64 v[166:167], v[166:167], 0, s[60:61]
	global_store_dwordx4 v[166:167], v[150:153], off
	v_lshl_add_u64 v[164:165], v[164:165], 0, s[36:37]
	global_load_dwordx4 v[62:65], v[164:165], off
	global_load_dwordx4 v[58:61], v[164:165], off offset:16
	v_cvt_f32_i32_e32 v54, v54
	v_cvt_f32_i32_e32 v55, v55
	v_cvt_f32_i32_e32 v56, v56
	v_cvt_f32_i32_e32 v57, v57
	v_cvt_f32_i32_e32 v50, v50
	v_cvt_f32_i32_e32 v51, v51
	v_cvt_f32_i32_e32 v52, v52
	v_cvt_f32_i32_e32 v53, v53
	s_waitcnt vmcnt(9)
	v_pk_mul_f32 v[54:55], v[240:241], v[54:55] op_sel_hi:[0,1]
	v_pk_mul_f32 v[56:57], v[240:241], v[56:57] op_sel_hi:[0,1]
	v_pk_mul_f32 v[50:51], v[240:241], v[50:51] op_sel_hi:[0,1]
	v_pk_mul_f32 v[52:53], v[240:241], v[52:53] op_sel_hi:[0,1]
	v_pk_fma_f32 v[54:55], v[184:185], v[54:55], v[86:87]
	v_pk_fma_f32 v[56:57], v[186:187], v[56:57], v[88:89]
	v_pk_fma_f32 v[50:51], v[188:189], v[50:51], v[82:83]
	v_pk_fma_f32 v[52:53], v[190:191], v[52:53], v[84:85]
	v_cvt_pk_bf16_f32 v244, v54, v55
	v_cvt_pk_bf16_f32 v245, v56, v57
	v_cvt_pk_bf16_f32 v246, v50, v51
	v_cvt_pk_bf16_f32 v247, v52, v53
	global_store_dwordx4 v[166:167], v[244:247], off offset:256
	global_load_dwordx4 v[54:57], v[164:165], off offset:512
	global_load_dwordx4 v[50:53], v[164:165], off offset:528
	v_cvt_f32_i32_e32 v46, v46
	v_cvt_f32_i32_e32 v47, v47
	v_cvt_f32_i32_e32 v48, v48
	v_cvt_f32_i32_e32 v49, v49
	v_cvt_f32_i32_e32 v42, v42
	v_cvt_f32_i32_e32 v43, v43
	v_cvt_f32_i32_e32 v44, v44
	v_cvt_f32_i32_e32 v45, v45
	v_mov_b32_e32 v240, v173
	s_waitcnt vmcnt(9)
	v_pk_mul_f32 v[46:47], v[240:241], v[46:47] op_sel_hi:[0,1]
	v_pk_mul_f32 v[48:49], v[240:241], v[48:49] op_sel_hi:[0,1]
	v_pk_mul_f32 v[42:43], v[240:241], v[42:43] op_sel_hi:[0,1]
	v_pk_mul_f32 v[44:45], v[240:241], v[44:45] op_sel_hi:[0,1]
	v_pk_fma_f32 v[46:47], v[176:177], v[46:47], v[78:79]
	v_pk_fma_f32 v[48:49], v[178:179], v[48:49], v[80:81]
	v_pk_fma_f32 v[42:43], v[180:181], v[42:43], v[74:75]
	v_pk_fma_f32 v[44:45], v[182:183], v[44:45], v[76:77]
	v_cvt_pk_bf16_f32 v150, v46, v47
	v_cvt_pk_bf16_f32 v151, v48, v49
	v_cvt_pk_bf16_f32 v152, v42, v43
	v_cvt_pk_bf16_f32 v153, v44, v45
	v_lshl_add_u64 v[166:167], v[166:167], 0, s[58:59]
	global_store_dwordx4 v[166:167], v[150:153], off
	v_lshl_add_u64 v[164:165], v[164:165], 0, s[36:37]
	global_load_dwordx4 v[46:49], v[164:165], off
	global_load_dwordx4 v[42:45], v[164:165], off offset:16
	v_cvt_f32_i32_e32 v38, v38
	v_cvt_f32_i32_e32 v39, v39
	v_cvt_f32_i32_e32 v40, v40
	v_cvt_f32_i32_e32 v41, v41
	v_cvt_f32_i32_e32 v34, v34
	v_cvt_f32_i32_e32 v35, v35
	v_cvt_f32_i32_e32 v36, v36
	v_cvt_f32_i32_e32 v37, v37
	s_waitcnt vmcnt(9)
	v_pk_mul_f32 v[38:39], v[240:241], v[38:39] op_sel_hi:[0,1]
	v_pk_mul_f32 v[40:41], v[240:241], v[40:41] op_sel_hi:[0,1]
	v_pk_mul_f32 v[34:35], v[240:241], v[34:35] op_sel_hi:[0,1]
	v_pk_mul_f32 v[36:37], v[240:241], v[36:37] op_sel_hi:[0,1]
	v_pk_fma_f32 v[38:39], v[184:185], v[38:39], v[70:71]
	v_pk_fma_f32 v[40:41], v[186:187], v[40:41], v[72:73]
	v_pk_fma_f32 v[34:35], v[188:189], v[34:35], v[66:67]
	v_pk_fma_f32 v[36:37], v[190:191], v[36:37], v[68:69]
	v_cvt_pk_bf16_f32 v244, v38, v39
	v_cvt_pk_bf16_f32 v245, v40, v41
	v_cvt_pk_bf16_f32 v246, v34, v35
	v_cvt_pk_bf16_f32 v247, v36, v37
	global_store_dwordx4 v[166:167], v[244:247], off offset:256
	global_load_dwordx4 v[38:41], v[164:165], off offset:512
	global_load_dwordx4 v[34:37], v[164:165], off offset:528
	v_cvt_f32_i32_e32 v30, v30
	v_cvt_f32_i32_e32 v31, v31
	v_cvt_f32_i32_e32 v32, v32
	v_cvt_f32_i32_e32 v33, v33
	v_cvt_f32_i32_e32 v26, v26
	v_cvt_f32_i32_e32 v27, v27
	v_cvt_f32_i32_e32 v28, v28
	v_cvt_f32_i32_e32 v29, v29
	v_mov_b32_e32 v240, v174
	s_waitcnt vmcnt(9)
	v_pk_mul_f32 v[30:31], v[240:241], v[30:31] op_sel_hi:[0,1]
	v_pk_mul_f32 v[32:33], v[240:241], v[32:33] op_sel_hi:[0,1]
	v_pk_mul_f32 v[26:27], v[240:241], v[26:27] op_sel_hi:[0,1]
	v_pk_mul_f32 v[28:29], v[240:241], v[28:29] op_sel_hi:[0,1]
	v_pk_fma_f32 v[30:31], v[176:177], v[30:31], v[62:63]
	v_pk_fma_f32 v[32:33], v[178:179], v[32:33], v[64:65]
	v_pk_fma_f32 v[26:27], v[180:181], v[26:27], v[58:59]
	v_pk_fma_f32 v[28:29], v[182:183], v[28:29], v[60:61]
	v_cvt_pk_bf16_f32 v150, v30, v31
	v_cvt_pk_bf16_f32 v151, v32, v33
	v_cvt_pk_bf16_f32 v152, v26, v27
	v_cvt_pk_bf16_f32 v153, v28, v29
	v_lshl_add_u64 v[166:167], v[166:167], 0, s[58:59]
	global_store_dwordx4 v[166:167], v[150:153], off
	v_cvt_f32_i32_e32 v22, v22
	v_cvt_f32_i32_e32 v23, v23
	v_cvt_f32_i32_e32 v24, v24
	v_cvt_f32_i32_e32 v25, v25
	v_cvt_f32_i32_e32 v18, v18
	v_cvt_f32_i32_e32 v19, v19
	v_cvt_f32_i32_e32 v20, v20
	v_cvt_f32_i32_e32 v21, v21
	s_waitcnt vmcnt(7)
	v_pk_mul_f32 v[22:23], v[240:241], v[22:23] op_sel_hi:[0,1]
	v_pk_mul_f32 v[24:25], v[240:241], v[24:25] op_sel_hi:[0,1]
	v_pk_mul_f32 v[18:19], v[240:241], v[18:19] op_sel_hi:[0,1]
	v_pk_mul_f32 v[20:21], v[240:241], v[20:21] op_sel_hi:[0,1]
	v_pk_fma_f32 v[22:23], v[184:185], v[22:23], v[54:55]
	v_pk_fma_f32 v[24:25], v[186:187], v[24:25], v[56:57]
	v_pk_fma_f32 v[18:19], v[188:189], v[18:19], v[50:51]
	v_pk_fma_f32 v[20:21], v[190:191], v[20:21], v[52:53]
	v_cvt_pk_bf16_f32 v244, v22, v23
	v_cvt_pk_bf16_f32 v245, v24, v25
	v_cvt_pk_bf16_f32 v246, v18, v19
	v_cvt_pk_bf16_f32 v247, v20, v21
	global_store_dwordx4 v[166:167], v[244:247], off offset:256
	v_cvt_f32_i32_e32 v14, v14
	v_cvt_f32_i32_e32 v15, v15
	v_cvt_f32_i32_e32 v16, v16
	v_cvt_f32_i32_e32 v17, v17
	v_cvt_f32_i32_e32 v10, v10
	v_cvt_f32_i32_e32 v11, v11
	v_cvt_f32_i32_e32 v12, v12
	v_cvt_f32_i32_e32 v13, v13
	v_mov_b32_e32 v240, v161
	s_waitcnt vmcnt(5)
	v_pk_mul_f32 v[14:15], v[240:241], v[14:15] op_sel_hi:[0,1]
	v_pk_mul_f32 v[16:17], v[240:241], v[16:17] op_sel_hi:[0,1]
	v_pk_mul_f32 v[10:11], v[240:241], v[10:11] op_sel_hi:[0,1]
	v_pk_mul_f32 v[12:13], v[240:241], v[12:13] op_sel_hi:[0,1]
	v_pk_fma_f32 v[14:15], v[176:177], v[14:15], v[46:47]
	v_pk_fma_f32 v[16:17], v[178:179], v[16:17], v[48:49]
	v_pk_fma_f32 v[10:11], v[180:181], v[10:11], v[42:43]
	v_pk_fma_f32 v[12:13], v[182:183], v[12:13], v[44:45]
	v_cvt_pk_bf16_f32 v150, v14, v15
	v_cvt_pk_bf16_f32 v151, v16, v17
	v_cvt_pk_bf16_f32 v152, v10, v11
	v_cvt_pk_bf16_f32 v153, v12, v13
	v_lshl_add_u64 v[166:167], v[166:167], 0, s[58:59]
	global_store_dwordx4 v[166:167], v[150:153], off
	v_cvt_f32_i32_e32 v6, v6
	v_cvt_f32_i32_e32 v7, v7
	v_cvt_f32_i32_e32 v8, v8
	v_cvt_f32_i32_e32 v9, v9
	v_cvt_f32_i32_e32 v2, v2
	v_cvt_f32_i32_e32 v3, v3
	v_cvt_f32_i32_e32 v4, v4
	v_cvt_f32_i32_e32 v5, v5
	s_waitcnt vmcnt(3)
	v_pk_mul_f32 v[6:7], v[240:241], v[6:7] op_sel_hi:[0,1]
	v_pk_mul_f32 v[8:9], v[240:241], v[8:9] op_sel_hi:[0,1]
	v_pk_mul_f32 v[2:3], v[240:241], v[2:3] op_sel_hi:[0,1]
	v_pk_mul_f32 v[4:5], v[240:241], v[4:5] op_sel_hi:[0,1]
	v_pk_fma_f32 v[6:7], v[184:185], v[6:7], v[38:39]
	v_pk_fma_f32 v[8:9], v[186:187], v[8:9], v[40:41]
	v_pk_fma_f32 v[2:3], v[188:189], v[2:3], v[34:35]
	v_pk_fma_f32 v[4:5], v[190:191], v[4:5], v[36:37]
	v_cvt_pk_bf16_f32 v244, v6, v7
	v_cvt_pk_bf16_f32 v245, v8, v9
	v_cvt_pk_bf16_f32 v246, v2, v3
	v_cvt_pk_bf16_f32 v247, v4, v5
	global_store_dwordx4 v[166:167], v[244:247], off offset:256
	s_andn2_b64 vcc, exec, s[2:3]
	s_mov_b64 s[2:3], -1
	v_readlane_b32 s82, v242, 13
	v_readlane_b32 s83, v242, 14
	v_readlane_b32 s84, v242, 15
	v_readlane_b32 s85, v242, 16
	v_readlane_b32 s86, v242, 17
	v_readlane_b32 s87, v242, 18
	v_readlane_b32 s88, v242, 19
	v_readlane_b32 s89, v242, 20
	v_readlane_b32 s90, v242, 21
	v_readlane_b32 s91, v242, 22
	v_readlane_b32 s92, v242, 23
	v_readlane_b32 s93, v242, 24
	v_readlane_b32 s94, v242, 25
	v_readlane_b32 s95, v242, 26
	s_cbranch_vccnz .LBB0_1224
	s_andn2_b64 vcc, exec, s[4:5]
	s_cbranch_vccnz .LBB0_1223
	s_barrier
	s_branch .LBB0_1223
